# attention tile loops: waves 4-7 staggered behind waves 0-3 by s_sleep 8 after each tile barrier so the two waves of a SIMD alternate MFMA and VALU phases
# speedup vs baseline: 1.0061x; 1.0061x over previous
.LBB0_1652:
	s_or_b64 exec, exec, s[8:9]
	s_barrier
	v_readfirstlane_b32 s101, v0
	s_bitcmp1_b32 s101, 8
	s_cbranch_scc0 .Lmy_stg_ma
	s_sleep 8
.Lmy_stg_ma:
	s_add_i32 s8, s17, 5
	v_cmp_lt_u32_e32 vcc, s8, v100
	s_and_saveexec_b64 s[8:9], vcc
	s_cbranch_execz .LBB0_1654
	s_lshl_b32 s10, s16, 14
	s_addk_i32 s10, 0xc000
	s_cmp_lg_u32 s16, 0
	s_cselect_b32 s10, s10, 0x14000
	v_add_u32_e32 v2, s10, v106
	v_add_u32_e32 v36, 0xc380, v2
	v_add_u32_e32 v2, 0xe380, v2
	v_readfirstlane_b32 s10, v36
	s_mov_b32 m0, s10
	v_readfirstlane_b32 s10, v2
	global_load_lds_dwordx4 v[88:89], off
	v_lshl_add_u64 v[36:37], s[50:51], 1, v[86:87]
	s_mov_b32 m0, s10
	s_nop 0
	global_load_lds_dwordx4 v[36:37], off

.LBB0_1707:
	s_or_b64 exec, exec, s[34:35]
	s_barrier
	v_readfirstlane_b32 s101, v0
	s_bitcmp1_b32 s101, 8
	s_cbranch_scc0 .Lmy_stg_dl
	s_sleep 8
.Lmy_stg_dl:
	s_add_i32 s34, s49, 5
	v_cmp_lt_u32_e32 vcc, s34, v147
	s_and_saveexec_b64 s[34:35], vcc
	s_cbranch_execz .LBB0_1709
	s_lshl_b32 s36, s46, 14
	s_addk_i32 s36, 0xc000
	s_cmp_lg_u32 s46, 0
	s_cselect_b32 s36, s36, 0x14000
	v_add_u32_e32 v2, s36, v151
	v_add_u32_e32 v36, 0x4100, v2
	v_add_u32_e32 v2, 0x6100, v2
	v_readfirstlane_b32 s36, v36
	s_mov_b32 m0, s36
	s_add_i32 s50, s47, 0xfffffe81
	v_readfirstlane_b32 s36, v2
	global_load_lds_dwordx4 v[128:129], off
	v_lshl_add_u64 v[36:37], s[50:51], 1, v[126:127]
	s_mov_b32 m0, s36
	s_nop 0
	global_load_lds_dwordx4 v[36:37], off
